# mLSTM-C unit: the 16 V-row loads issued with the Q/K tile loads (one round trip instead of three), V loop unrolled
# baseline (speedup 1.0000x reference)
.LBB0_649:
	v_cmp_gt_u32_e32 vcc, s62, v86
	v_lshlrev_b32_e32 v41, 4, v86
	v_bfe_u32 v1, v86, 4, 6
	v_cndmask_b32_e32 v82, v93, v94, vcc
	v_lshl_add_u64 v[34:35], s[18:19], 0, v[82:83]
	v_and_b32_e32 v82, 0xf0, v41
	v_add_u32_e32 v41, 0x200, v86
	v_or_b32_e32 v36, s40, v1
	v_bfe_u32 v48, v41, 4, 6
	v_ashrrev_i32_e32 v37, 31, v36
	s_lshl_b32 s26, s2, 8
	v_cmp_gt_u32_e64 s[2:3], s62, v41
	v_or_b32_e32 v44, s40, v48
	v_lshlrev_b64 v[36:37], 10, v[36:37]
	v_cndmask_b32_e64 v42, v93, v94, s[2:3]
	v_mov_b32_e32 v43, v83
	v_ashrrev_i32_e32 v45, 31, v44
	v_lshl_add_u64 v[34:35], v[34:35], 0, v[36:37]
	v_lshl_add_u64 v[42:43], s[18:19], 0, v[42:43]
	v_lshlrev_b64 v[44:45], 10, v[44:45]
	v_lshl_add_u64 v[34:35], v[34:35], 0, s[26:27]
	v_lshl_add_u64 v[42:43], v[42:43], 0, v[44:45]
	v_lshl_add_u64 v[34:35], v[34:35], 0, v[82:83]
	v_lshl_add_u64 v[42:43], v[42:43], 0, s[26:27]
	v_cmp_lt_u32_e64 s[4:5], s66, v86
	v_lshl_add_u64 v[42:43], v[42:43], 0, v[82:83]
	global_load_dwordx4 v[44:47], v[34:35], off
	global_load_dwordx4 v[68:71], v[42:43], off
	v_cndmask_b32_e64 v34, v93, v94, s[4:5]
	v_mov_b32_e32 v35, v83
	v_lshl_add_u64 v[34:35], s[18:19], 0, v[34:35]
	v_lshl_add_u64 v[34:35], v[34:35], 0, v[36:37]
	v_add_u32_e32 v36, 0x600, v86
	v_bfe_u32 v49, v36, 4, 6
	v_cmp_gt_u32_e64 s[6:7], s62, v36
	v_or_b32_e32 v42, s40, v49
	v_mov_b32_e32 v37, v83
	v_cndmask_b32_e64 v36, v93, v94, s[6:7]
	v_ashrrev_i32_e32 v43, 31, v42
	v_lshl_add_u64 v[36:37], s[18:19], 0, v[36:37]
	v_lshlrev_b64 v[42:43], 10, v[42:43]
	v_lshl_add_u64 v[34:35], v[34:35], 0, s[26:27]
	v_lshl_add_u64 v[36:37], v[36:37], 0, v[42:43]
	v_lshl_add_u64 v[34:35], v[34:35], 0, v[82:83]
	v_lshl_add_u64 v[36:37], v[36:37], 0, s[26:27]
	v_lshl_add_u64 v[36:37], v[36:37], 0, v[82:83]
	global_load_dwordx4 v[72:75], v[34:35], off
	global_load_dwordx4 v[76:79], v[36:37], off
	v_mov_b32_e32 v35, s64
	v_mov_b32_e32 v36, s63
	v_ashrrev_i32_e32 v98, 3, v86
	v_lshlrev_b32_e32 v37, 1, v86
	v_cndmask_b32_e32 v42, v35, v36, vcc
	v_mul_u32_u24_e32 v1, 0x110, v1
	v_cndmask_b32_e64 v43, v35, v36, s[4:5]
	v_and_b32_e32 v41, 0xfe, v37
	v_lshlrev_b32_e32 v37, 1, v98
	s_load_dwordx2 s[38:39], s[38:39], 0x0
	v_add3_u32 v67, v42, v1, v82
	v_cndmask_b32_e64 v80, v35, v36, s[2:3]
	v_add3_u32 v1, v43, v1, v82
	v_cndmask_b32_e64 v36, v35, v36, s[6:7]
	v_mul_u32_u24_e32 v43, 0x110, v49
	v_mad_u32_u24 v35, v41, s67, 0
	v_and_b32_e32 v42, 0xffffffe0, v37
	v_mul_u32_u24_e32 v48, 0x110, v48
	v_add3_u32 v36, v36, v43, v82
	v_add_u32_e32 v43, v35, v42
	v_add3_u32 v37, v80, v48, v82
	v_add_u32_e32 v48, 0x9000, v43
	v_add_u32_e32 v49, 0x901e, v43
	v_add_u32_e32 v80, 0x9090, v43
	v_add_u32_e32 v43, 0x90ae, v43
	v_cmp_ge_u32_e32 vcc, v49, v48
	v_cmp_ge_u32_e64 s[2:3], v43, v80
	v_and_b32_e32 v34, -16, v98
	s_and_b64 s[2:3], vcc, s[2:3]
	s_lshl_b32 s6, s26, 1
	s_add_u32 s6, s10, s6
	s_addc_u32 s7, s11, 0
	v_lshlrev_b32_e32 v158, 2, v0
	v_and_b32_e32 v158, 0x1fc, v158
	v_mov_b32_e32 v159, 0
	v_lshl_add_u64 v[160:161], s[6:7], 0, v[158:159]
	v_ashrrev_i32_e32 v158, 3, v0
	v_and_b32_e32 v158, -16, v158
	v_add_u32_e32 v158, s40, v158
	v_mad_i64_i32 v[162:163], s[6:7], v158, s68, v[160:161]
	s_mov_b32 s6, 0x3000
	s_mov_b32 s7, 0
	global_load_dword v142, v[162:163], off offset:2048
	v_lshl_add_u64 v[162:163], v[162:163], 0, s[6:7]
	global_load_dword v143, v[162:163], off offset:2048
	v_lshl_add_u64 v[162:163], v[162:163], 0, s[6:7]
	global_load_dword v144, v[162:163], off offset:2048
	v_lshl_add_u64 v[162:163], v[162:163], 0, s[6:7]
	global_load_dword v145, v[162:163], off offset:2048
	v_lshl_add_u64 v[162:163], v[162:163], 0, s[6:7]
	global_load_dword v146, v[162:163], off offset:2048
	v_lshl_add_u64 v[162:163], v[162:163], 0, s[6:7]
	global_load_dword v147, v[162:163], off offset:2048
	v_lshl_add_u64 v[162:163], v[162:163], 0, s[6:7]
	global_load_dword v148, v[162:163], off offset:2048
	v_lshl_add_u64 v[162:163], v[162:163], 0, s[6:7]
	global_load_dword v149, v[162:163], off offset:2048
	v_lshl_add_u64 v[162:163], v[162:163], 0, s[6:7]
	global_load_dword v150, v[162:163], off offset:2048
	v_lshl_add_u64 v[162:163], v[162:163], 0, s[6:7]
	global_load_dword v151, v[162:163], off offset:2048
	v_lshl_add_u64 v[162:163], v[162:163], 0, s[6:7]
	global_load_dword v152, v[162:163], off offset:2048
	v_lshl_add_u64 v[162:163], v[162:163], 0, s[6:7]
	global_load_dword v153, v[162:163], off offset:2048
	v_lshl_add_u64 v[162:163], v[162:163], 0, s[6:7]
	global_load_dword v154, v[162:163], off offset:2048
	v_lshl_add_u64 v[162:163], v[162:163], 0, s[6:7]
	global_load_dword v155, v[162:163], off offset:2048
	v_lshl_add_u64 v[162:163], v[162:163], 0, s[6:7]
	global_load_dword v156, v[162:163], off offset:2048
	v_lshl_add_u64 v[162:163], v[162:163], 0, s[6:7]
	global_load_dword v157, v[162:163], off offset:2048
	s_waitcnt vmcnt(0)
	ds_write_b128 v67, v[44:47]
	ds_write_b128 v37, v[68:71]
	ds_write_b128 v1, v[72:75]
	ds_write_b128 v36, v[76:79]
	s_and_saveexec_b64 s[4:5], s[2:3]
	s_xor_b64 s[2:3], exec, s[4:5]
	s_cbranch_execz .LBB0_652
	s_lshl_b32 s6, s26, 1
	s_add_u32 s6, s10, s6
	s_addc_u32 s7, s11, 0
	v_lshlrev_b32_e32 v82, 1, v41
	v_mov_b32_e32 v1, v34
	s_mov_b32 s4, s40
	s_mov_b32 s5, 1
	v_lshl_add_u64 v[36:37], s[6:7], 0, v[82:83]
	s_mov_b32 s6, 0
	s_mov_b32 s7, 16
	v_or_b32_e32 v67, s6, v34
	v_or_b32_e32 v41, s5, v1
	s_add_i32 s37, s5, 2
	s_add_i32 s41, s6, 2
	s_add_i32 s82, s5, 4
	s_add_i32 s83, s6, 4
	v_add_u32_e32 v42, s40, v67
	s_add_i32 s84, s5, 6
	s_add_i32 s85, s6, 6
	v_add_u32_e32 v41, s4, v41
	v_or_b32_e32 v46, s37, v1
	v_or_b32_e32 v72, s41, v34
	v_or_b32_e32 v47, s82, v1
	v_or_b32_e32 v73, s83, v34
	v_mad_i64_i32 v[42:43], s[82:83], v42, s68, v[36:37]
	v_or_b32_e32 v48, s84, v1
	v_or_b32_e32 v74, s85, v34
	v_mad_i64_i32 v[44:45], s[82:83], v41, s68, v[36:37]
	v_add_u32_e32 v41, s4, v46
	v_add_u32_e32 v46, s40, v72
	v_add_u32_e32 v49, s4, v47
	v_add_u32_e32 v47, s40, v73
	v_mov_b32_e32 v75, v142
	v_mov_b32_e32 v76, v143
	v_add_u32_e32 v70, s4, v48
	v_add_u32_e32 v68, s40, v74
	v_mad_i64_i32 v[42:43], s[82:83], v46, s68, v[36:37]
	v_mad_i64_i32 v[44:45], s[82:83], v41, s68, v[36:37]
	v_mad_i64_i32 v[46:47], s[82:83], v47, s68, v[36:37]
	v_mad_i64_i32 v[48:49], s[82:83], v49, s68, v[36:37]
	v_mad_i64_i32 v[68:69], s[82:83], v68, s68, v[36:37]
	v_mad_i64_i32 v[70:71], s[82:83], v70, s68, v[36:37]
	v_mov_b32_e32 v43, v144
	s_nop 0
	v_mov_b32_e32 v44, v145
	s_nop 0
	v_mov_b32_e32 v45, v146
	s_nop 0
	v_mov_b32_e32 v46, v147
	v_mov_b32_e32 v47, v148
	s_nop 0
	v_mov_b32_e32 v48, v149
	v_lshl_add_u32 v49, v67, 1, v35
	s_add_i32 s6, s6, 8
	s_add_i32 s5, s5, 8
	s_add_i32 s7, s7, -8
	v_add_u32_e32 v49, 0x9000, v49
	v_lshl_add_u32 v67, v72, 1, v35
	s_cmp_lg_u32 s7, 0
	v_lshl_add_u32 v68, v73, 1, v35
	v_lshl_add_u32 v69, v74, 1, v35
	v_add_u32_e32 v67, 0x9000, v67
	v_add_u32_e32 v68, 0x9000, v68
	v_add_u32_e32 v69, 0x9000, v69
	v_perm_b32 v70, v76, v75, s69
	v_perm_b32 v71, v76, v75, s70
	ds_write2_b32 v49, v70, v71 offset1:36
	v_perm_b32 v49, v44, v43, s69
	v_perm_b32 v43, v44, v43, s70
	v_perm_b32 v44, v46, v45, s69
	v_perm_b32 v45, v46, v45, s70
	v_perm_b32 v46, v48, v47, s69
	v_perm_b32 v47, v48, v47, s70
	ds_write2_b32 v67, v49, v43 offset1:36
	ds_write2_b32 v68, v44, v45 offset1:36
	ds_write2_b32 v69, v46, v47 offset1:36
	v_or_b32_e32 v67, s6, v34
	v_or_b32_e32 v41, s5, v1
	s_add_i32 s37, s5, 2
	s_add_i32 s41, s6, 2
	s_add_i32 s82, s5, 4
	s_add_i32 s83, s6, 4
	v_add_u32_e32 v42, s40, v67
	s_add_i32 s84, s5, 6
	s_add_i32 s85, s6, 6
	v_add_u32_e32 v41, s4, v41
	v_or_b32_e32 v46, s37, v1
	v_or_b32_e32 v72, s41, v34
	v_or_b32_e32 v47, s82, v1
	v_or_b32_e32 v73, s83, v34
	v_mad_i64_i32 v[42:43], s[82:83], v42, s68, v[36:37]
	v_or_b32_e32 v48, s84, v1
	v_or_b32_e32 v74, s85, v34
	v_mad_i64_i32 v[44:45], s[82:83], v41, s68, v[36:37]
	v_add_u32_e32 v41, s4, v46
	v_add_u32_e32 v46, s40, v72
	v_add_u32_e32 v49, s4, v47
	v_add_u32_e32 v47, s40, v73
	v_mov_b32_e32 v75, v150
	v_mov_b32_e32 v76, v151
	v_add_u32_e32 v70, s4, v48
	v_add_u32_e32 v68, s40, v74
	v_mad_i64_i32 v[42:43], s[82:83], v46, s68, v[36:37]
	v_mad_i64_i32 v[44:45], s[82:83], v41, s68, v[36:37]
	v_mad_i64_i32 v[46:47], s[82:83], v47, s68, v[36:37]
	v_mad_i64_i32 v[48:49], s[82:83], v49, s68, v[36:37]
	v_mad_i64_i32 v[68:69], s[82:83], v68, s68, v[36:37]
	v_mad_i64_i32 v[70:71], s[82:83], v70, s68, v[36:37]
	v_mov_b32_e32 v43, v152
	s_nop 0
	v_mov_b32_e32 v44, v153
	s_nop 0
	v_mov_b32_e32 v45, v154
	s_nop 0
	v_mov_b32_e32 v46, v155
	v_mov_b32_e32 v47, v156
	s_nop 0
	v_mov_b32_e32 v48, v157
	v_lshl_add_u32 v49, v67, 1, v35
	s_add_i32 s6, s6, 8
	s_add_i32 s5, s5, 8
	s_add_i32 s7, s7, -8
	v_add_u32_e32 v49, 0x9000, v49
	v_lshl_add_u32 v67, v72, 1, v35
	s_cmp_lg_u32 s7, 0
	v_lshl_add_u32 v68, v73, 1, v35
	v_lshl_add_u32 v69, v74, 1, v35
	v_add_u32_e32 v67, 0x9000, v67
	v_add_u32_e32 v68, 0x9000, v68
	v_add_u32_e32 v69, 0x9000, v69
	v_perm_b32 v70, v76, v75, s69
	v_perm_b32 v71, v76, v75, s70
	ds_write2_b32 v49, v70, v71 offset1:36
	v_perm_b32 v49, v44, v43, s69
	v_perm_b32 v43, v44, v43, s70
	v_perm_b32 v44, v46, v45, s69
	v_perm_b32 v45, v46, v45, s70
	v_perm_b32 v46, v48, v47, s69
	v_perm_b32 v47, v48, v47, s70
	ds_write2_b32 v67, v49, v43 offset1:36
	ds_write2_b32 v68, v44, v45 offset1:36
	ds_write2_b32 v69, v46, v47 offset1:36
